# v12: + P1 K-tile-t+1 side-job finish/issue moved into its MFMA block (m1)
# baseline (speedup 1.0000x reference)
.Lp1vg_mmafter_b:
	s_barrier
	s_mov_b32 m0, s69
	v_lshl_add_u64 v[4:5], v[4:5], 0, s[24:25]
	s_add_u32 s4, s56, 0x80080
	ds_read_b128 v[174:177], v234 offset:49152
	ds_read_b128 v[178:181], v234 offset:50176
	ds_read_b128 v[182:185], v234 offset:51200
	ds_read_b128 v[186:189], v234 offset:52224
	ds_read_b128 v[190:193], v234 offset:53248
	ds_read_b128 v[194:197], v234 offset:54272
	ds_read_b128 v[198:201], v234 offset:55296
	ds_read_b128 v[202:205], v234 offset:56320
	global_load_lds_dwordx4 v[4:5], off
	v_lshl_add_u64 v[4:5], v[226:227], 0, s[24:25]
	s_mov_b32 m0, s70
	s_addc_u32 s5, s57, 0
	global_load_lds_dwordx4 v[4:5], off
	v_lshl_add_u64 v[4:5], s[4:5], 0, v[212:213]
	s_mov_b32 m0, s73
	s_nop 0
	global_load_lds_dwordx4 v[4:5], off
	v_lshl_add_u64 v[4:5], s[4:5], 0, v[216:217]
	s_mov_b32 m0, s75
	s_nop 0
	global_load_lds_dwordx4 v[4:5], off
	v_lshl_add_u64 v[4:5], v[228:229], 0, s[24:25]
	s_mov_b32 m0, s71
	s_nop 0
	global_load_lds_dwordx4 v[4:5], off
	v_lshl_add_u64 v[4:5], v[230:231], 0, s[24:25]
	s_mov_b32 m0, s72
	s_nop 0
	global_load_lds_dwordx4 v[4:5], off
	s_cmp_eq_u32 s100, 3
	s_cbranch_scc1 .Lp1vg_w11_b2
	s_waitcnt vmcnt(8)
	s_branch .Lp1vg_wd_b2

;     __device__ __forceinline__ void finish(v4i_t& t0, v4i_t& t1, int j, int tid) const {
;         asm volatile("" : "+v"(t0), "+v"(t1));
;         const float* s0; unsigned char* d; addr(j, tid, s0, d);
;         const f32x4 r0 = __builtin_bit_cast(f32x4, t0) * 64.f, r1 = __builtin_bit_cast(f32x4, t1) * 64.f;
;         int w0 = 0, w1 = 0; w0 = __builtin_amdgcn_cvt_pk_fp8_f32(r0[0], r1[0], w0, false); w0 = __builtin_amdgcn_cvt_pk_fp8_f32(r0[1], r1[1], w0, true);
;         w1 = __builtin_amdgcn_cvt_pk_fp8_f32(r0[2], r1[2], w1, false); w1 = __builtin_amdgcn_cvt_pk_fp8_f32(r0[3], r1[3], w1, true);
;         typedef int v2is __attribute__((ext_vector_type(2))); __builtin_nontemporal_store((v2is){w0, w1}, (v2is*)d);
.Lp1vg_wd_b1:
	s_waitcnt lgkmcnt(0)
	s_cmp_lt_i32 s99, 0
	s_cbranch_scc1 .Lp1vg_mmslow_b
	s_cmpk_gt_i32 s77, 0x5f
	s_cbranch_scc1 .Lp1vg_mmslow_b
	s_barrier
	s_setprio 1
	s_waitcnt lgkmcnt(0)
	v_mfma_f32_16x16x32_bf16 v[138:141], v[158:161], v[198:201], v[138:141]
	s_add_i32 s4, s99, s68
	s_lshr_b32 s2, s4, 31
	s_add_i32 s2, s4, s2
	v_mfma_f32_16x16x32_bf16 v[134:137], v[166:169], v[198:201], v[134:137]
	s_ashr_i32 s5, s2, 1
	s_ashr_i32 s2, s2, 11
	s_and_b32 s3, s5, 0x3ff
	v_mfma_f32_16x16x32_bf16 v[122:125], v[158:161], v[190:193], v[122:125]
	s_ashr_i32 s82, s2, 31
	s_lshl_b32 s2, s2, 10
	v_pk_mul_f32 v[240:241], v[240:241], s[40:41] op_sel_hi:[1,0]
	v_mfma_f32_16x16x32_bf16 v[118:121], v[166:169], v[190:193], v[118:121]
	v_pk_mul_f32 v[242:243], v[242:243], s[40:41] op_sel_hi:[1,0]
	v_pk_mul_f32 v[244:245], v[244:245], s[40:41] op_sel_hi:[1,0]
	v_pk_mul_f32 v[246:247], v[246:247], s[40:41] op_sel_hi:[1,0]
	v_mfma_f32_16x16x32_bf16 v[106:109], v[158:161], v[182:185], v[106:109]
	s_or_b32 s2, s2, s3
	v_cvt_pk_fp8_f32 v240, v240, v244
	s_mul_hi_u32 s3, s2, 0x2100
	v_mfma_f32_16x16x32_bf16 v[102:105], v[166:169], v[182:185], v[102:105]
	s_mulk_i32 s82, 0x2100
	v_cvt_pk_fp8_f32 v240, v241, v245 op_sel:[0,0,1]
	s_add_i32 s3, s3, s82
	v_mfma_f32_16x16x32_bf16 v[90:93], v[158:161], v[174:177], v[90:93]
	s_mulk_i32 s2, 0x2100
	v_cvt_pk_fp8_f32 v241, v242, v246
	v_readlane_b32 s101, v251, 49
	v_mfma_f32_16x16x32_bf16 v[86:89], v[166:169], v[174:177], v[86:89]
	s_add_u32 s2, s101, s2
	v_readlane_b32 s101, v251, 31
	s_addc_u32 s3, s101, s3
	v_mfma_f32_16x16x32_bf16 v[138:141], v[162:165], v[202:205], v[138:141]
	v_cvt_pk_fp8_f32 v241, v243, v247 op_sel:[0,0,1]
	v_lshl_or_b32 v248, s4, 11, v208
	s_lshl_b32 s82, s5, 12
	v_mfma_f32_16x16x32_bf16 v[134:137], v[170:173], v[202:205], v[134:137]
	v_subrev_u32_e32 v238, s82, v248
	v_ashrrev_i32_e32 v239, 31, v238
	v_lshl_add_u64 v[238:239], v[238:239], 1, s[2:3]
	v_mfma_f32_16x16x32_bf16 v[122:125], v[162:165], v[194:197], v[122:125]
	global_store_dwordx2 v[238:239], v[240:241], off nt
	s_add_i32 s4, s77, s68
	s_lshr_b32 s2, s4, 31
	v_mfma_f32_16x16x32_bf16 v[118:121], v[170:173], v[194:197], v[118:121]
	s_add_i32 s2, s4, s2
	s_ashr_i32 s5, s2, 1
	s_ashr_i32 s2, s2, 11
	v_mfma_f32_16x16x32_bf16 v[106:109], v[162:165], v[186:189], v[106:109]
	s_ashr_i32 s3, s2, 31
	s_lshl_b64 s[2:3], s[2:3], 25
	v_readlane_b32 s84, v251, 36
	v_mfma_f32_16x16x32_bf16 v[102:105], v[170:173], v[186:189], v[102:105]
	v_readlane_b32 s85, v251, 37
	s_add_u32 s2, s84, s2
	s_addc_u32 s3, s85, s3
	v_mfma_f32_16x16x32_bf16 v[90:93], v[162:165], v[178:181], v[90:93]
	s_lshl_b32 s84, s5, 15
	s_and_b32 s84, s84, 0x1ff8000
	s_add_u32 s84, s2, s84
	s_addc_u32 s85, s3, 0
	v_mfma_f32_16x16x32_bf16 v[86:89], v[170:173], v[178:181], v[86:89]
	s_setprio 0
	s_setprio 1
	s_lshl_b32 s2, s5, 12
	s_lshl_b32 s3, s4, 11
	s_sub_i32 s2, s3, s2
	v_mfma_f32_16x16x32_bf16 v[130:133], v[142:145], v[198:201], v[130:133]
	s_ashr_i32 s3, s2, 31
	s_lshl_b64 s[2:3], s[2:3], 2
	s_add_u32 s2, s84, s2
	s_addc_u32 s3, s85, s3
	v_mfma_f32_16x16x32_bf16 v[126:129], v[150:153], v[198:201], v[126:129]
	v_lshlrev_b32_e32 v2, 2, v208
	v_lshl_add_u64 v[238:239], s[2:3], 0, v[2:3]
	v_lshl_add_u64 v[238:239], v[238:239], 0, s[42:43]
	v_mfma_f32_16x16x32_bf16 v[114:117], v[142:145], v[190:193], v[114:117]
	global_load_dwordx4 v[240:243], v2, s[2:3] nt
	global_load_dwordx4 v[244:247], v[238:239], off nt
	s_mov_b32 s100, 3
	v_mfma_f32_16x16x32_bf16 v[110:113], v[150:153], v[190:193], v[110:113]
	s_mov_b32 s99, s77
	s_add_i32 s77, s77, 1
	v_mfma_f32_16x16x32_bf16 v[98:101], v[142:145], v[182:185], v[98:101]
	v_mfma_f32_16x16x32_bf16 v[94:97], v[150:153], v[182:185], v[94:97]
	v_mfma_f32_16x16x32_bf16 v[82:85], v[142:145], v[174:177], v[82:85]
	v_mfma_f32_16x16x32_bf16 v[78:81], v[150:153], v[174:177], v[78:81]
	v_mfma_f32_16x16x32_bf16 v[130:133], v[146:149], v[202:205], v[130:133]
	v_mfma_f32_16x16x32_bf16 v[126:129], v[154:157], v[202:205], v[126:129]
	v_mfma_f32_16x16x32_bf16 v[114:117], v[146:149], v[194:197], v[114:117]
	v_mfma_f32_16x16x32_bf16 v[110:113], v[154:157], v[194:197], v[110:113]
	v_mfma_f32_16x16x32_bf16 v[98:101], v[146:149], v[186:189], v[98:101]
	v_mfma_f32_16x16x32_bf16 v[94:97], v[154:157], v[186:189], v[94:97]
	v_mfma_f32_16x16x32_bf16 v[82:85], v[146:149], v[178:181], v[82:85]
	v_mfma_f32_16x16x32_bf16 v[78:81], v[154:157], v[178:181], v[78:81]
	s_setprio 0
	s_branch .Lp1vg_mmafter_b
.Lp1vg_mmslow_b:
	s_mov_b32 s100, 0
	s_cmp_lt_i32 s99, 0
	s_cbranch_scc1 .Lp1vg_nf_b
	s_add_i32 s4, s99, s68
	s_lshr_b32 s2, s4, 31
	s_add_i32 s2, s4, s2
	s_ashr_i32 s5, s2, 1
	s_ashr_i32 s2, s2, 11
	s_and_b32 s3, s5, 0x3ff
	s_ashr_i32 s82, s2, 31
	s_lshl_b32 s2, s2, 10
	v_pk_mul_f32 v[240:241], v[240:241], s[40:41] op_sel_hi:[1,0]
	v_pk_mul_f32 v[242:243], v[242:243], s[40:41] op_sel_hi:[1,0]
	v_pk_mul_f32 v[244:245], v[244:245], s[40:41] op_sel_hi:[1,0]
	v_pk_mul_f32 v[246:247], v[246:247], s[40:41] op_sel_hi:[1,0]
	s_or_b32 s2, s2, s3
	v_cvt_pk_fp8_f32 v240, v240, v244
	s_mul_hi_u32 s3, s2, 0x2100
	s_mulk_i32 s82, 0x2100
	v_cvt_pk_fp8_f32 v240, v241, v245 op_sel:[0,0,1]
	s_add_i32 s3, s3, s82
	s_mulk_i32 s2, 0x2100
	v_cvt_pk_fp8_f32 v241, v242, v246
	v_readlane_b32 s101, v251, 49
	s_add_u32 s2, s101, s2
	v_readlane_b32 s101, v251, 31
	s_addc_u32 s3, s101, s3
	v_cvt_pk_fp8_f32 v241, v243, v247 op_sel:[0,0,1]
	v_lshl_or_b32 v248, s4, 11, v208
	s_lshl_b32 s82, s5, 12
	v_subrev_u32_e32 v238, s82, v248
	v_ashrrev_i32_e32 v239, 31, v238
	v_lshl_add_u64 v[238:239], v[238:239], 1, s[2:3]
	global_store_dwordx2 v[238:239], v[240:241], off nt
	s_mov_b32 s100, 1
